# attention<16> epilogue: fp8 O tile transposed through free LDS, 16 scattered dword stores -> 4 coalesced dwordx4 stores
# speedup vs baseline: 1.0309x; 1.0006x over previous
.LBB0_1280:
	v_mbcnt_lo_u32_b32 v196, -1, 0
	v_mbcnt_hi_u32_b32 v196, -1, v196
	s_mul_i32 s60, s95, 0x50
	v_and_b32_e32 v197, 15, v196
	v_lshrrev_b32_e32 v203, 4, v196
	v_mul_u32_u24_e32 v194, 0x90, v197
	v_lshrrev_b32_e32 v202, 3, v196
	v_lshl_add_u32 v194, v203, 2, v194
	v_sub_u32_e32 v197, v202, v197
	v_mul_u32_u24_e32 v195, 0x90, v202
	v_and_b32_e32 v202, 7, v196
	v_lshlrev_b32_e32 v197, 11, v197
	v_lshl_add_u32 v195, v202, 4, v195
	v_lshl_add_u32 v202, v202, 4, v197
	v_lshlrev_b32_e32 v203, 2, v203
	v_add_u32_e32 v194, s60, v194
	v_sub_u32_e32 v202, v202, v203
	v_add_u32_e32 v195, s60, v195
	v_ashrrev_i32_e32 v203, 31, v202
	v_add_u32_e32 v194, 0x18000, v194
	v_add_u32_e32 v195, 0x18000, v195
	s_mov_b64 s[60:61], 0x4000
	s_xor_b64 s[8:9], s[6:7], -1
	v_div_scale_f32 v70, s[6:7], v103, v103, 1.0
	v_rcp_f32_e32 v71, v70
	v_div_scale_f32 v72, vcc, 1.0, v103, 1.0
	v_ashrrev_i32_e32 v215, 31, v214
	v_fma_f32 v73, -v70, v71, 1.0
	v_fmac_f32_e32 v71, v73, v71
	v_mul_f32_e32 v73, v72, v71
	v_fma_f32 v74, -v70, v73, v72
	v_fmac_f32_e32 v73, v74, v71
	v_fma_f32 v70, -v70, v73, v72
	v_div_fmas_f32 v70, v70, v71, v73
	v_div_fixup_f32 v70, v70, v103, 1.0
	v_pk_mul_f32 v[66:67], v[66:67], v[70:71] op_sel_hi:[1,0]
	v_mov_b32_e32 v71, v33
	v_cvt_pk_fp8_f32 v71, v66, v67
	v_lshlrev_b64 v[66:67], 11, v[214:215]
	v_ashrrev_i32_e32 v213, 31, v212
	v_pk_mul_f32 v[68:69], v[68:69], v[70:71] op_sel_hi:[1,0]
	s_nop 0
	v_cvt_pk_fp8_f32 v71, v68, v69 op_sel:[0,0,1]
	v_mov_b32_e32 v68, v33
	v_pk_mul_f32 v[62:63], v[70:71], v[62:63] op_sel_hi:[0,1]
	v_cvt_pk_fp8_f32 v68, v62, v63
	v_pk_mul_f32 v[58:59], v[70:71], v[58:59] op_sel_hi:[0,1]
	v_mov_b32_e32 v62, v33
	v_cvt_pk_fp8_f32 v62, v58, v59
	v_pk_mul_f32 v[58:59], v[70:71], v[64:65] op_sel_hi:[0,1]
	v_cvt_pk_fp8_f32 v68, v58, v59 op_sel:[0,0,1]
	v_pk_mul_f32 v[58:59], v[70:71], v[60:61] op_sel_hi:[0,1]
	v_pk_mul_f32 v[54:55], v[70:71], v[54:55] op_sel_hi:[0,1]
	v_mov_b32_e32 v60, v33
	v_cvt_pk_fp8_f32 v60, v54, v55
	v_pk_mul_f32 v[50:51], v[70:71], v[50:51] op_sel_hi:[0,1]
	v_mov_b32_e32 v54, v33
	v_cvt_pk_fp8_f32 v54, v50, v51
	v_pk_mul_f32 v[50:51], v[70:71], v[56:57] op_sel_hi:[0,1]
	v_cvt_pk_fp8_f32 v60, v50, v51 op_sel:[0,0,1]
	v_pk_mul_f32 v[50:51], v[70:71], v[52:53] op_sel_hi:[0,1]
	v_cvt_pk_fp8_f32 v54, v50, v51 op_sel:[0,0,1]
	v_pk_mul_f32 v[46:47], v[70:71], v[46:47] op_sel_hi:[0,1]
	v_mov_b32_e32 v50, v33
	v_cvt_pk_fp8_f32 v50, v46, v47
	v_pk_mul_f32 v[46:47], v[70:71], v[48:49] op_sel_hi:[0,1]
	v_pk_mul_f32 v[38:39], v[70:71], v[38:39] op_sel_hi:[0,1]
	v_cvt_pk_fp8_f32 v62, v58, v59 op_sel:[0,0,1]
	v_cvt_pk_fp8_f32 v50, v46, v47 op_sel:[0,0,1]
	v_mov_b32_e32 v46, v33
	v_cvt_pk_fp8_f32 v46, v38, v39
	v_pk_mul_f32 v[38:39], v[70:71], v[42:43] op_sel_hi:[0,1]
	v_mov_b32_e32 v42, v33
	v_cvt_pk_fp8_f32 v42, v38, v39
	v_pk_mul_f32 v[38:39], v[70:71], v[40:41] op_sel_hi:[0,1]
	v_cvt_pk_fp8_f32 v46, v38, v39 op_sel:[0,0,1]
	v_pk_mul_f32 v[38:39], v[70:71], v[44:45] op_sel_hi:[0,1]
	v_cvt_pk_fp8_f32 v42, v38, v39 op_sel:[0,0,1]
	v_div_scale_f32 v38, s[6:7], v102, v102, 1.0
	v_rcp_f32_e32 v39, v38
	v_lshl_add_u64 v[58:59], v[192:193], 0, v[66:67]
	ds_write_b32 v194, v71
	ds_write_b32 v194, v68 offset:16
	ds_write_b32 v194, v62 offset:32
	ds_write_b32 v194, v60 offset:48
	ds_write_b32 v194, v54 offset:64
	v_fma_f32 v40, -v38, v39, 1.0
	v_fmac_f32_e32 v39, v40, v39
	v_div_scale_f32 v40, vcc, 1.0, v102, 1.0
	v_mul_f32_e32 v41, v40, v39
	ds_write_b32 v194, v50 offset:80
	ds_write_b32 v194, v46 offset:96
	ds_write_b32 v194, v42 offset:112
	v_fma_f32 v42, -v38, v41, v40
	v_fmac_f32_e32 v41, v42, v39
	v_fma_f32 v38, -v38, v41, v40
	v_div_fmas_f32 v38, v38, v39, v41
	v_div_fixup_f32 v38, v38, v102, 1.0
	v_pk_mul_f32 v[28:29], v[38:39], v[28:29] op_sel_hi:[0,1]
	v_mov_b32_e32 v39, v33
	v_cvt_pk_fp8_f32 v39, v28, v29
	v_mov_b32_e32 v28, v33
	v_lshlrev_b64 v[40:41], 11, v[212:213]
	v_lshl_add_u64 v[40:41], v[192:193], 0, v[40:41]
	v_pk_mul_f32 v[24:25], v[38:39], v[24:25] op_sel_hi:[0,1]
	v_cvt_pk_fp8_f32 v28, v24, v25
	v_pk_mul_f32 v[24:25], v[38:39], v[30:31] op_sel_hi:[0,1]
	v_cvt_pk_fp8_f32 v39, v24, v25 op_sel:[0,0,1]
	s_mov_b64 s[6:7], 0
	s_and_b64 vcc, exec, s[8:9]
	v_pk_mul_f32 v[24:25], v[38:39], v[26:27] op_sel_hi:[0,1]
	v_cvt_pk_fp8_f32 v28, v24, v25 op_sel:[0,0,1]
	v_pk_mul_f32 v[20:21], v[38:39], v[20:21] op_sel_hi:[0,1]
	v_mov_b32_e32 v24, v33
	v_cvt_pk_fp8_f32 v24, v20, v21
	v_pk_mul_f32 v[16:17], v[38:39], v[16:17] op_sel_hi:[0,1]
	v_mov_b32_e32 v20, v33
	v_cvt_pk_fp8_f32 v20, v16, v17
	v_pk_mul_f32 v[16:17], v[38:39], v[22:23] op_sel_hi:[0,1]
	v_cvt_pk_fp8_f32 v24, v16, v17 op_sel:[0,0,1]
	v_pk_mul_f32 v[16:17], v[38:39], v[18:19] op_sel_hi:[0,1]
	v_cvt_pk_fp8_f32 v20, v16, v17 op_sel:[0,0,1]
	v_pk_mul_f32 v[12:13], v[38:39], v[12:13] op_sel_hi:[0,1]
	v_mov_b32_e32 v16, v33
	v_cvt_pk_fp8_f32 v16, v12, v13
	v_pk_mul_f32 v[8:9], v[38:39], v[8:9] op_sel_hi:[0,1]
	v_mov_b32_e32 v12, v33
	v_cvt_pk_fp8_f32 v12, v8, v9
	v_pk_mul_f32 v[8:9], v[38:39], v[14:15] op_sel_hi:[0,1]
	v_cvt_pk_fp8_f32 v16, v8, v9 op_sel:[0,0,1]
	v_pk_mul_f32 v[8:9], v[38:39], v[10:11] op_sel_hi:[0,1]
	v_cvt_pk_fp8_f32 v12, v8, v9 op_sel:[0,0,1]
	v_pk_mul_f32 v[4:5], v[38:39], v[4:5] op_sel_hi:[0,1]
	v_mov_b32_e32 v8, v33
	v_cvt_pk_fp8_f32 v8, v4, v5
	v_pk_mul_f32 v[0:1], v[38:39], v[0:1] op_sel_hi:[0,1]
	v_mov_b32_e32 v4, v33
	v_cvt_pk_fp8_f32 v4, v0, v1
	v_pk_mul_f32 v[0:1], v[38:39], v[6:7] op_sel_hi:[0,1]
	v_cvt_pk_fp8_f32 v8, v0, v1 op_sel:[0,0,1]
	v_pk_mul_f32 v[0:1], v[38:39], v[2:3] op_sel_hi:[0,1]
	v_cvt_pk_fp8_f32 v4, v0, v1 op_sel:[0,0,1]
	ds_write_b32 v194, v39 offset:2304
	ds_write_b32 v194, v28 offset:2320
	ds_write_b32 v194, v24 offset:2336
	ds_write_b32 v194, v20 offset:2352
	ds_write_b32 v194, v16 offset:2368
	ds_write_b32 v194, v12 offset:2384
	ds_write_b32 v194, v8 offset:2400
	ds_write_b32 v194, v4 offset:2416
	ds_read_b128 v[0:3], v195
	ds_read_b128 v[4:7], v195 offset:1152
	ds_read_b128 v[8:11], v195 offset:2304
	ds_read_b128 v[12:15], v195 offset:3456
	v_lshl_add_u64 v[196:197], v[58:59], 0, v[202:203]
	s_waitcnt lgkmcnt(0)
	global_store_dwordx4 v[196:197], v[0:3], off
	v_lshl_add_u64 v[196:197], v[196:197], 0, s[60:61]
	global_store_dwordx4 v[196:197], v[4:7], off
	v_lshl_add_u64 v[196:197], v[196:197], 0, s[60:61]
	global_store_dwordx4 v[196:197], v[8:11], off
	v_lshl_add_u64 v[196:197], v[196:197], 0, s[60:61]
	global_store_dwordx4 v[196:197], v[12:15], off
	s_nop 1
	s_cbranch_vccnz .LBB0_1278
